# baseline (speedup 1.0000x reference)
_Z8dog_mainPKfS0_S0_S0_S0_S0_S0_Pf:
	s_load_dwordx8 s[12:19], s[0:1], 0x0
	s_load_dwordx8 s[20:27], s[0:1], 0x20
	s_and_b32 s3, s2, 7
	s_lshl_b32 s3, s3, 5
	s_lshr_b32 s4, s2, 3
	s_add_i32 s4, s3, s4
	s_and_b32 s6, s4, 3
	s_lshr_b32 s7, s4, 2
	s_mov_b32 s5, 0
	s_lshl_b64 s[8:9], s[4:5], 18
	v_and_b32_e32 v1, 63, v0
	v_lshrrev_b32_e32 v2, 6, v0
	v_and_b32_e32 v3, 31, v0
	v_lshl_or_b32 v4, v2, 5, v3
	v_lshlrev_b32_e32 v5, 2, v4
	v_lshlrev_b32_e32 v6, 4, v1
	v_lshl_or_b32 v6, v2, 12, v6
	s_waitcnt lgkmcnt(0)
	global_load_dword v20, v5, s[18:19]
	global_load_dword v21, v5, s[20:21]
	global_load_dword v22, v5, s[22:23]
	global_load_dword v23, v5, s[24:25]
	global_load_dword v24, v5, s[14:15]
	global_load_dword v25, v5, s[16:17]
	s_add_u32 s12, s12, s8
	s_addc_u32 s13, s13, s9
	global_load_dwordx4 v[128:131], v6, s[12:13] offset:0 nt
	global_load_dwordx4 v[132:135], v6, s[12:13] offset:1024 nt
	global_load_dwordx4 v[136:139], v6, s[12:13] offset:2048 nt
	global_load_dwordx4 v[140:143], v6, s[12:13] offset:3072 nt
	v_add_u32_e32 v6, 0x8000, v6
	global_load_dwordx4 v[144:147], v6, s[12:13] offset:0 nt
	global_load_dwordx4 v[148:151], v6, s[12:13] offset:1024 nt
	global_load_dwordx4 v[152:155], v6, s[12:13] offset:2048 nt
	global_load_dwordx4 v[156:159], v6, s[12:13] offset:3072 nt
	v_bfe_u32 v7, v0, 5, 1
	v_and_b32_e32 v16, 1, v0
	v_cmp_eq_u32_e64 s[30:31], 0, v16
	v_and_b32_e32 v17, 2, v0
	v_cmp_eq_u32_e64 s[32:33], 0, v17
	v_and_b32_e32 v16, 3, v0
	v_lshrrev_b32_e32 v17, 2, v1
	v_lshlrev_b32_e32 v16, 5, v16
	v_lshl_add_u32 v16, v17, 1, v16
	v_lshrrev_b32_e32 v17, 1, v2
	s_movk_i32 s10, 0x110
	v_mad_u32_u24 v16, v17, s10, v16
	v_and_b32_e32 v17, 1, v2
	v_lshl_add_u32 v14, v17, 7, v16
	v_lshlrev_b32_e32 v17, 4, v7
	v_mad_u32_u24 v15, v3, s10, v17
	s_lshl_b32 s11, s6, 5
	v_lshl_add_u32 v18, v7, 2, s11
	v_cvt_f32_u32_e32 v18, v18
	v_lshlrev_b32_e32 v19, 3, v7
	v_cvt_f32_u32_e32 v19, v19
	s_waitcnt vmcnt(8)
	v_add_f32_e32 v26, v20, v21
	v_rcp_f32_e32 v27, v20
	v_rcp_f32_e32 v28, v26
	v_sub_f32_e32 v12, v19, v22
	v_sub_f32_e32 v13, v18, v23
	v_fma_f32 v29, -v20, v27, 1.0
	v_fma_f32 v30, -v26, v28, 1.0
	v_fma_f32 v27, v29, v27, v27
	v_fma_f32 v28, v30, v28, v28
	v_mul_f32_e32 v8, 0xbf38aa3b, v27
	v_mul_f32_e32 v9, 0xbf38aa3b, v28
	v_mul_f32_e32 v29, v24, v27
	v_mul_f32_e32 v30, v25, v28
	v_mul_f32_e32 v10, 0x3e22f983, v29
	v_mul_f32_e32 v11, 0x3e22f983, v30
	v_mul_f32_e32 v16, v12, v12
	v_add_f32_e32 v17, 0x3f800000, v12
	v_add_f32_e32 v18, 0x40000000, v12
	v_add_f32_e32 v19, 0x40400000, v12
	v_mul_f32_e32 v17, v17, v17
	v_mul_f32_e32 v18, v18, v18
	v_mul_f32_e32 v19, v19, v19
	v_mul_f32_e32 v20, v8, v16
	v_mul_f32_e32 v24, v9, v16
	v_mul_f32_e32 v21, v8, v17
	v_mul_f32_e32 v25, v9, v17
	v_mul_f32_e32 v22, v8, v18
	v_mul_f32_e32 v26, v9, v18
	v_mul_f32_e32 v23, v8, v19
	v_mul_f32_e32 v27, v9, v19
	v_exp_f32_e32 v20, v20
	v_exp_f32_e32 v21, v21
	v_exp_f32_e32 v22, v22
	v_exp_f32_e32 v23, v23
	v_exp_f32_e32 v24, v24
	v_exp_f32_e32 v25, v25
	v_exp_f32_e32 v26, v26
	v_exp_f32_e32 v27, v27
	v_cvt_pk_f16_f32 v32, v20, v21
	v_cvt_pk_f16_f32 v33, v22, v23
	v_cvt_pk_f16_f32 v64, v24, v25
	v_cvt_pk_f16_f32 v65, v26, v27
	v_add_f32_e32 v16, 0x40800000, v12
	v_add_f32_e32 v17, 0x40a00000, v12
	v_add_f32_e32 v18, 0x40c00000, v12
	v_add_f32_e32 v19, 0x40e00000, v12
	v_mul_f32_e32 v16, v16, v16
	v_mul_f32_e32 v17, v17, v17
	v_mul_f32_e32 v18, v18, v18
	v_mul_f32_e32 v19, v19, v19
	v_mul_f32_e32 v20, v8, v16
	v_mul_f32_e32 v24, v9, v16
	v_mul_f32_e32 v21, v8, v17
	v_mul_f32_e32 v25, v9, v17
	v_mul_f32_e32 v22, v8, v18
	v_mul_f32_e32 v26, v9, v18
	v_mul_f32_e32 v23, v8, v19
	v_mul_f32_e32 v27, v9, v19
	v_exp_f32_e32 v20, v20
	v_exp_f32_e32 v21, v21
	v_exp_f32_e32 v22, v22
	v_exp_f32_e32 v23, v23
	v_exp_f32_e32 v24, v24
	v_exp_f32_e32 v25, v25
	v_exp_f32_e32 v26, v26
	v_exp_f32_e32 v27, v27
	v_cvt_pk_f16_f32 v34, v20, v21
	v_cvt_pk_f16_f32 v35, v22, v23
	v_cvt_pk_f16_f32 v66, v24, v25
	v_cvt_pk_f16_f32 v67, v26, v27
	v_add_f32_e32 v16, 0x41800000, v12
	v_add_f32_e32 v17, 0x41880000, v12
	v_add_f32_e32 v18, 0x41900000, v12
	v_add_f32_e32 v19, 0x41980000, v12
	v_mul_f32_e32 v16, v16, v16
	v_mul_f32_e32 v17, v17, v17
	v_mul_f32_e32 v18, v18, v18
	v_mul_f32_e32 v19, v19, v19
	v_mul_f32_e32 v20, v8, v16
	v_mul_f32_e32 v24, v9, v16
	v_mul_f32_e32 v21, v8, v17
	v_mul_f32_e32 v25, v9, v17
	v_mul_f32_e32 v22, v8, v18
	v_mul_f32_e32 v26, v9, v18
	v_mul_f32_e32 v23, v8, v19
	v_mul_f32_e32 v27, v9, v19
	v_exp_f32_e32 v20, v20
	v_exp_f32_e32 v21, v21
	v_exp_f32_e32 v22, v22
	v_exp_f32_e32 v23, v23
	v_exp_f32_e32 v24, v24
	v_exp_f32_e32 v25, v25
	v_exp_f32_e32 v26, v26
	v_exp_f32_e32 v27, v27
	v_cvt_pk_f16_f32 v36, v20, v21
	v_cvt_pk_f16_f32 v37, v22, v23
	v_cvt_pk_f16_f32 v68, v24, v25
	v_cvt_pk_f16_f32 v69, v26, v27
	v_add_f32_e32 v16, 0x41a00000, v12
	v_add_f32_e32 v17, 0x41a80000, v12
	v_add_f32_e32 v18, 0x41b00000, v12
	v_add_f32_e32 v19, 0x41b80000, v12
	v_mul_f32_e32 v16, v16, v16
	v_mul_f32_e32 v17, v17, v17
	v_mul_f32_e32 v18, v18, v18
	v_mul_f32_e32 v19, v19, v19
	v_mul_f32_e32 v20, v8, v16
	v_mul_f32_e32 v24, v9, v16
	v_mul_f32_e32 v21, v8, v17
	v_mul_f32_e32 v25, v9, v17
	v_mul_f32_e32 v22, v8, v18
	v_mul_f32_e32 v26, v9, v18
	v_mul_f32_e32 v23, v8, v19
	v_mul_f32_e32 v27, v9, v19
	v_exp_f32_e32 v20, v20
	v_exp_f32_e32 v21, v21
	v_exp_f32_e32 v22, v22
	v_exp_f32_e32 v23, v23
	v_exp_f32_e32 v24, v24
	v_exp_f32_e32 v25, v25
	v_exp_f32_e32 v26, v26
	v_exp_f32_e32 v27, v27
	v_cvt_pk_f16_f32 v38, v20, v21
	v_cvt_pk_f16_f32 v39, v22, v23
	v_cvt_pk_f16_f32 v70, v24, v25
	v_cvt_pk_f16_f32 v71, v26, v27
	v_add_u32_e32 v6, 0x8000, v6
	global_load_dwordx4 v[160:163], v6, s[12:13] offset:0 nt
	global_load_dwordx4 v[164:167], v6, s[12:13] offset:1024 nt
	global_load_dwordx4 v[168:171], v6, s[12:13] offset:2048 nt
	global_load_dwordx4 v[172:175], v6, s[12:13] offset:3072 nt
	v_add_f32_e32 v16, 0x42000000, v12
	v_add_f32_e32 v17, 0x42040000, v12
	v_add_f32_e32 v18, 0x42080000, v12
	v_add_f32_e32 v19, 0x420c0000, v12
	v_mul_f32_e32 v16, v16, v16
	v_mul_f32_e32 v17, v17, v17
	v_mul_f32_e32 v18, v18, v18
	v_mul_f32_e32 v19, v19, v19
	v_mul_f32_e32 v20, v8, v16
	v_mul_f32_e32 v24, v9, v16
	v_mul_f32_e32 v21, v8, v17
	v_mul_f32_e32 v25, v9, v17
	v_mul_f32_e32 v22, v8, v18
	v_mul_f32_e32 v26, v9, v18
	v_mul_f32_e32 v23, v8, v19
	v_mul_f32_e32 v27, v9, v19
	v_exp_f32_e32 v20, v20
	v_exp_f32_e32 v21, v21
	v_exp_f32_e32 v22, v22
	v_exp_f32_e32 v23, v23
	v_exp_f32_e32 v24, v24
	v_exp_f32_e32 v25, v25
	v_exp_f32_e32 v26, v26
	v_exp_f32_e32 v27, v27
	v_cvt_pk_f16_f32 v40, v20, v21
	v_cvt_pk_f16_f32 v41, v22, v23
	v_cvt_pk_f16_f32 v72, v24, v25
	v_cvt_pk_f16_f32 v73, v26, v27
	v_add_f32_e32 v16, 0x42100000, v12
	v_add_f32_e32 v17, 0x42140000, v12
	v_add_f32_e32 v18, 0x42180000, v12
	v_add_f32_e32 v19, 0x421c0000, v12
	v_mul_f32_e32 v16, v16, v16
	v_mul_f32_e32 v17, v17, v17
	v_mul_f32_e32 v18, v18, v18
	v_mul_f32_e32 v19, v19, v19
	v_mul_f32_e32 v20, v8, v16
	v_mul_f32_e32 v24, v9, v16
	v_mul_f32_e32 v21, v8, v17
	v_mul_f32_e32 v25, v9, v17
	v_mul_f32_e32 v22, v8, v18
	v_mul_f32_e32 v26, v9, v18
	v_mul_f32_e32 v23, v8, v19
	v_mul_f32_e32 v27, v9, v19
	v_exp_f32_e32 v20, v20
	v_exp_f32_e32 v21, v21
	v_exp_f32_e32 v22, v22
	v_exp_f32_e32 v23, v23
	v_exp_f32_e32 v24, v24
	v_exp_f32_e32 v25, v25
	v_exp_f32_e32 v26, v26
	v_exp_f32_e32 v27, v27
	v_cvt_pk_f16_f32 v42, v20, v21
	v_cvt_pk_f16_f32 v43, v22, v23
	v_cvt_pk_f16_f32 v74, v24, v25
	v_cvt_pk_f16_f32 v75, v26, v27
	v_add_f32_e32 v16, 0x42400000, v12
	v_add_f32_e32 v17, 0x42440000, v12
	v_add_f32_e32 v18, 0x42480000, v12
	v_add_f32_e32 v19, 0x424c0000, v12
	v_mul_f32_e32 v16, v16, v16
	v_mul_f32_e32 v17, v17, v17
	v_mul_f32_e32 v18, v18, v18
	v_mul_f32_e32 v19, v19, v19
	v_mul_f32_e32 v20, v8, v16
	v_mul_f32_e32 v24, v9, v16
	v_mul_f32_e32 v21, v8, v17
	v_mul_f32_e32 v25, v9, v17
	v_mul_f32_e32 v22, v8, v18
	v_mul_f32_e32 v26, v9, v18
	v_mul_f32_e32 v23, v8, v19
	v_mul_f32_e32 v27, v9, v19
	v_exp_f32_e32 v20, v20
	v_exp_f32_e32 v21, v21
	v_exp_f32_e32 v22, v22
	v_exp_f32_e32 v23, v23
	v_exp_f32_e32 v24, v24
	v_exp_f32_e32 v25, v25
	v_exp_f32_e32 v26, v26
	v_exp_f32_e32 v27, v27
	v_cvt_pk_f16_f32 v44, v20, v21
	v_cvt_pk_f16_f32 v45, v22, v23
	v_cvt_pk_f16_f32 v76, v24, v25
	v_cvt_pk_f16_f32 v77, v26, v27
	v_add_f32_e32 v16, 0x42500000, v12
	v_add_f32_e32 v17, 0x42540000, v12
	v_add_f32_e32 v18, 0x42580000, v12
	v_add_f32_e32 v19, 0x425c0000, v12
	v_mul_f32_e32 v16, v16, v16
	v_mul_f32_e32 v17, v17, v17
	v_mul_f32_e32 v18, v18, v18
	v_mul_f32_e32 v19, v19, v19
	v_mul_f32_e32 v20, v8, v16
	v_mul_f32_e32 v24, v9, v16
	v_mul_f32_e32 v21, v8, v17
	v_mul_f32_e32 v25, v9, v17
	v_mul_f32_e32 v22, v8, v18
	v_mul_f32_e32 v26, v9, v18
	v_mul_f32_e32 v23, v8, v19
	v_mul_f32_e32 v27, v9, v19
	v_exp_f32_e32 v20, v20
	v_exp_f32_e32 v21, v21
	v_exp_f32_e32 v22, v22
	v_exp_f32_e32 v23, v23
	v_exp_f32_e32 v24, v24
	v_exp_f32_e32 v25, v25
	v_exp_f32_e32 v26, v26
	v_exp_f32_e32 v27, v27
	v_cvt_pk_f16_f32 v46, v20, v21
	v_cvt_pk_f16_f32 v47, v22, v23
	v_cvt_pk_f16_f32 v78, v24, v25
	v_cvt_pk_f16_f32 v79, v26, v27
	v_add_u32_e32 v6, 0x8000, v6
	global_load_dwordx4 v[176:179], v6, s[12:13] offset:0 nt
	global_load_dwordx4 v[180:183], v6, s[12:13] offset:1024 nt
	global_load_dwordx4 v[184:187], v6, s[12:13] offset:2048 nt
	global_load_dwordx4 v[188:191], v6, s[12:13] offset:3072 nt
	v_add_f32_e32 v16, 0x42800000, v12
	v_add_f32_e32 v17, 0x42820000, v12
	v_add_f32_e32 v18, 0x42840000, v12
	v_add_f32_e32 v19, 0x42860000, v12
	v_mul_f32_e32 v16, v16, v16
	v_mul_f32_e32 v17, v17, v17
	v_mul_f32_e32 v18, v18, v18
	v_mul_f32_e32 v19, v19, v19
	v_mul_f32_e32 v20, v8, v16
	v_mul_f32_e32 v24, v9, v16
	v_mul_f32_e32 v21, v8, v17
	v_mul_f32_e32 v25, v9, v17
	v_mul_f32_e32 v22, v8, v18
	v_mul_f32_e32 v26, v9, v18
	v_mul_f32_e32 v23, v8, v19
	v_mul_f32_e32 v27, v9, v19
	v_exp_f32_e32 v20, v20
	v_exp_f32_e32 v21, v21
	v_exp_f32_e32 v22, v22
	v_exp_f32_e32 v23, v23
	v_exp_f32_e32 v24, v24
	v_exp_f32_e32 v25, v25
	v_exp_f32_e32 v26, v26
	v_exp_f32_e32 v27, v27
	v_cvt_pk_f16_f32 v48, v20, v21
	v_cvt_pk_f16_f32 v49, v22, v23
	v_cvt_pk_f16_f32 v80, v24, v25
	v_cvt_pk_f16_f32 v81, v26, v27
	v_add_f32_e32 v16, 0x42880000, v12
	v_add_f32_e32 v17, 0x428a0000, v12
	v_add_f32_e32 v18, 0x428c0000, v12
	v_add_f32_e32 v19, 0x428e0000, v12
	v_mul_f32_e32 v16, v16, v16
	v_mul_f32_e32 v17, v17, v17
	v_mul_f32_e32 v18, v18, v18
	v_mul_f32_e32 v19, v19, v19
	v_mul_f32_e32 v20, v8, v16
	v_mul_f32_e32 v24, v9, v16
	v_mul_f32_e32 v21, v8, v17
	v_mul_f32_e32 v25, v9, v17
	v_mul_f32_e32 v22, v8, v18
	v_mul_f32_e32 v26, v9, v18
	v_mul_f32_e32 v23, v8, v19
	v_mul_f32_e32 v27, v9, v19
	v_exp_f32_e32 v20, v20
	v_exp_f32_e32 v21, v21
	v_exp_f32_e32 v22, v22
	v_exp_f32_e32 v23, v23
	v_exp_f32_e32 v24, v24
	v_exp_f32_e32 v25, v25
	v_exp_f32_e32 v26, v26
	v_exp_f32_e32 v27, v27
	v_cvt_pk_f16_f32 v50, v20, v21
	v_cvt_pk_f16_f32 v51, v22, v23
	v_cvt_pk_f16_f32 v82, v24, v25
	v_cvt_pk_f16_f32 v83, v26, v27
	v_add_f32_e32 v16, 0x42a00000, v12
	v_add_f32_e32 v17, 0x42a20000, v12
	v_add_f32_e32 v18, 0x42a40000, v12
	v_add_f32_e32 v19, 0x42a60000, v12
	v_mul_f32_e32 v16, v16, v16
	v_mul_f32_e32 v17, v17, v17
	v_mul_f32_e32 v18, v18, v18
	v_mul_f32_e32 v19, v19, v19
	v_mul_f32_e32 v20, v8, v16
	v_mul_f32_e32 v24, v9, v16
	v_mul_f32_e32 v21, v8, v17
	v_mul_f32_e32 v25, v9, v17
	v_mul_f32_e32 v22, v8, v18
	v_mul_f32_e32 v26, v9, v18
	v_mul_f32_e32 v23, v8, v19
	v_mul_f32_e32 v27, v9, v19
	v_exp_f32_e32 v20, v20
	v_exp_f32_e32 v21, v21
	v_exp_f32_e32 v22, v22
	v_exp_f32_e32 v23, v23
	v_exp_f32_e32 v24, v24
	v_exp_f32_e32 v25, v25
	v_exp_f32_e32 v26, v26
	v_exp_f32_e32 v27, v27
	v_cvt_pk_f16_f32 v52, v20, v21
	v_cvt_pk_f16_f32 v53, v22, v23
	v_cvt_pk_f16_f32 v84, v24, v25
	v_cvt_pk_f16_f32 v85, v26, v27
	v_add_f32_e32 v16, 0x42a80000, v12
	v_add_f32_e32 v17, 0x42aa0000, v12
	v_add_f32_e32 v18, 0x42ac0000, v12
	v_add_f32_e32 v19, 0x42ae0000, v12
	v_mul_f32_e32 v16, v16, v16
	v_mul_f32_e32 v17, v17, v17
	v_mul_f32_e32 v18, v18, v18
	v_mul_f32_e32 v19, v19, v19
	v_mul_f32_e32 v20, v8, v16
	v_mul_f32_e32 v24, v9, v16
	v_mul_f32_e32 v21, v8, v17
	v_mul_f32_e32 v25, v9, v17
	v_mul_f32_e32 v22, v8, v18
	v_mul_f32_e32 v26, v9, v18
	v_mul_f32_e32 v23, v8, v19
	v_mul_f32_e32 v27, v9, v19
	v_exp_f32_e32 v20, v20
	v_exp_f32_e32 v21, v21
	v_exp_f32_e32 v22, v22
	v_exp_f32_e32 v23, v23
	v_exp_f32_e32 v24, v24
	v_exp_f32_e32 v25, v25
	v_exp_f32_e32 v26, v26
	v_exp_f32_e32 v27, v27
	v_cvt_pk_f16_f32 v54, v20, v21
	v_cvt_pk_f16_f32 v55, v22, v23
	v_cvt_pk_f16_f32 v86, v24, v25
	v_cvt_pk_f16_f32 v87, v26, v27
	v_add_u32_e32 v6, 0x8000, v6
	global_load_dwordx4 v[192:195], v6, s[12:13] offset:0 nt
	global_load_dwordx4 v[196:199], v6, s[12:13] offset:1024 nt
	global_load_dwordx4 v[200:203], v6, s[12:13] offset:2048 nt
	global_load_dwordx4 v[204:207], v6, s[12:13] offset:3072 nt
	v_add_f32_e32 v16, 0x42c00000, v12
	v_add_f32_e32 v17, 0x42c20000, v12
	v_add_f32_e32 v18, 0x42c40000, v12
	v_add_f32_e32 v19, 0x42c60000, v12
	v_mul_f32_e32 v16, v16, v16
	v_mul_f32_e32 v17, v17, v17
	v_mul_f32_e32 v18, v18, v18
	v_mul_f32_e32 v19, v19, v19
	v_mul_f32_e32 v20, v8, v16
	v_mul_f32_e32 v24, v9, v16
	v_mul_f32_e32 v21, v8, v17
	v_mul_f32_e32 v25, v9, v17
	v_mul_f32_e32 v22, v8, v18
	v_mul_f32_e32 v26, v9, v18
	v_mul_f32_e32 v23, v8, v19
	v_mul_f32_e32 v27, v9, v19
	v_exp_f32_e32 v20, v20
	v_exp_f32_e32 v21, v21
	v_exp_f32_e32 v22, v22
	v_exp_f32_e32 v23, v23
	v_exp_f32_e32 v24, v24
	v_exp_f32_e32 v25, v25
	v_exp_f32_e32 v26, v26
	v_exp_f32_e32 v27, v27
	v_cvt_pk_f16_f32 v56, v20, v21
	v_cvt_pk_f16_f32 v57, v22, v23
	v_cvt_pk_f16_f32 v88, v24, v25
	v_cvt_pk_f16_f32 v89, v26, v27
	v_add_f32_e32 v16, 0x42c80000, v12
	v_add_f32_e32 v17, 0x42ca0000, v12
	v_add_f32_e32 v18, 0x42cc0000, v12
	v_add_f32_e32 v19, 0x42ce0000, v12
	v_mul_f32_e32 v16, v16, v16
	v_mul_f32_e32 v17, v17, v17
	v_mul_f32_e32 v18, v18, v18
	v_mul_f32_e32 v19, v19, v19
	v_mul_f32_e32 v20, v8, v16
	v_mul_f32_e32 v24, v9, v16
	v_mul_f32_e32 v21, v8, v17
	v_mul_f32_e32 v25, v9, v17
	v_mul_f32_e32 v22, v8, v18
	v_mul_f32_e32 v26, v9, v18
	v_mul_f32_e32 v23, v8, v19
	v_mul_f32_e32 v27, v9, v19
	v_exp_f32_e32 v20, v20
	v_exp_f32_e32 v21, v21
	v_exp_f32_e32 v22, v22
	v_exp_f32_e32 v23, v23
	v_exp_f32_e32 v24, v24
	v_exp_f32_e32 v25, v25
	v_exp_f32_e32 v26, v26
	v_exp_f32_e32 v27, v27
	v_cvt_pk_f16_f32 v58, v20, v21
	v_cvt_pk_f16_f32 v59, v22, v23
	v_cvt_pk_f16_f32 v90, v24, v25
	v_cvt_pk_f16_f32 v91, v26, v27
	v_add_f32_e32 v16, 0x42e00000, v12
	v_add_f32_e32 v17, 0x42e20000, v12
	v_add_f32_e32 v18, 0x42e40000, v12
	v_add_f32_e32 v19, 0x42e60000, v12
	v_mul_f32_e32 v16, v16, v16
	v_mul_f32_e32 v17, v17, v17
	v_mul_f32_e32 v18, v18, v18
	v_mul_f32_e32 v19, v19, v19
	v_mul_f32_e32 v20, v8, v16
	v_mul_f32_e32 v24, v9, v16
	v_mul_f32_e32 v21, v8, v17
	v_mul_f32_e32 v25, v9, v17
	v_mul_f32_e32 v22, v8, v18
	v_mul_f32_e32 v26, v9, v18
	v_mul_f32_e32 v23, v8, v19
	v_mul_f32_e32 v27, v9, v19
	v_exp_f32_e32 v20, v20
	v_exp_f32_e32 v21, v21
	v_exp_f32_e32 v22, v22
	v_exp_f32_e32 v23, v23
	v_exp_f32_e32 v24, v24
	v_exp_f32_e32 v25, v25
	v_exp_f32_e32 v26, v26
	v_exp_f32_e32 v27, v27
	v_cvt_pk_f16_f32 v60, v20, v21
	v_cvt_pk_f16_f32 v61, v22, v23
	v_cvt_pk_f16_f32 v92, v24, v25
	v_cvt_pk_f16_f32 v93, v26, v27
	v_add_f32_e32 v16, 0x42e80000, v12
	v_add_f32_e32 v17, 0x42ea0000, v12
	v_add_f32_e32 v18, 0x42ec0000, v12
	v_add_f32_e32 v19, 0x42ee0000, v12
	v_mul_f32_e32 v16, v16, v16
	v_mul_f32_e32 v17, v17, v17
	v_mul_f32_e32 v18, v18, v18
	v_mul_f32_e32 v19, v19, v19
	v_mul_f32_e32 v20, v8, v16
	v_mul_f32_e32 v24, v9, v16
	v_mul_f32_e32 v21, v8, v17
	v_mul_f32_e32 v25, v9, v17
	v_mul_f32_e32 v22, v8, v18
	v_mul_f32_e32 v26, v9, v18
	v_mul_f32_e32 v23, v8, v19
	v_mul_f32_e32 v27, v9, v19
	v_exp_f32_e32 v20, v20
	v_exp_f32_e32 v21, v21
	v_exp_f32_e32 v22, v22
	v_exp_f32_e32 v23, v23
	v_exp_f32_e32 v24, v24
	v_exp_f32_e32 v25, v25
	v_exp_f32_e32 v26, v26
	v_exp_f32_e32 v27, v27
	v_cvt_pk_f16_f32 v62, v20, v21
	v_cvt_pk_f16_f32 v63, v22, v23
	v_cvt_pk_f16_f32 v94, v24, v25
	v_cvt_pk_f16_f32 v95, v26, v27
	v_add_u32_e32 v6, 0x8000, v6
	global_load_dwordx4 v[208:211], v6, s[12:13] offset:0 nt
	global_load_dwordx4 v[212:215], v6, s[12:13] offset:1024 nt
	global_load_dwordx4 v[216:219], v6, s[12:13] offset:2048 nt
	global_load_dwordx4 v[220:223], v6, s[12:13] offset:3072 nt
	v_mul_f32_e32 v16, v13, v13
	v_add_f32_e32 v17, 0x3f800000, v13
	v_add_f32_e32 v18, 0x40000000, v13
	v_add_f32_e32 v19, 0x40400000, v13
	v_mul_f32_e32 v17, v17, v17
	v_mul_f32_e32 v18, v18, v18
	v_mul_f32_e32 v19, v19, v19
	v_mul_f32_e32 v20, v8, v16
	v_mul_f32_e32 v24, v9, v16
	v_mul_f32_e32 v21, v8, v17
	v_mul_f32_e32 v25, v9, v17
	v_mul_f32_e32 v22, v8, v18
	v_mul_f32_e32 v26, v9, v18
	v_mul_f32_e32 v23, v8, v19
	v_mul_f32_e32 v27, v9, v19
	v_exp_f32_e32 v20, v20
	v_exp_f32_e32 v21, v21
	v_exp_f32_e32 v22, v22
	v_exp_f32_e32 v23, v23
	v_exp_f32_e32 v24, v24
	v_exp_f32_e32 v25, v25
	v_exp_f32_e32 v26, v26
	v_exp_f32_e32 v27, v27
	v_mul_f32_e32 v96, v10, v20
	v_mul_f32_e32 v97, v10, v21
	v_mul_f32_e32 v98, v10, v22
	v_mul_f32_e32 v99, v10, v23
	v_mul_f32_e32 v112, v11, v24
	v_mul_f32_e32 v113, v11, v25
	v_mul_f32_e32 v114, v11, v26
	v_mul_f32_e32 v115, v11, v27
	v_add_f32_e32 v16, 0x41000000, v13
	v_add_f32_e32 v17, 0x41100000, v13
	v_add_f32_e32 v18, 0x41200000, v13
	v_add_f32_e32 v19, 0x41300000, v13
	v_mul_f32_e32 v16, v16, v16
	v_mul_f32_e32 v17, v17, v17
	v_mul_f32_e32 v18, v18, v18
	v_mul_f32_e32 v19, v19, v19
	v_mul_f32_e32 v20, v8, v16
	v_mul_f32_e32 v24, v9, v16
	v_mul_f32_e32 v21, v8, v17
	v_mul_f32_e32 v25, v9, v17
	v_mul_f32_e32 v22, v8, v18
	v_mul_f32_e32 v26, v9, v18
	v_mul_f32_e32 v23, v8, v19
	v_mul_f32_e32 v27, v9, v19
	v_exp_f32_e32 v20, v20
	v_exp_f32_e32 v21, v21
	v_exp_f32_e32 v22, v22
	v_exp_f32_e32 v23, v23
	v_exp_f32_e32 v24, v24
	v_exp_f32_e32 v25, v25
	v_exp_f32_e32 v26, v26
	v_exp_f32_e32 v27, v27
	v_mul_f32_e32 v100, v10, v20
	v_mul_f32_e32 v101, v10, v21
	v_mul_f32_e32 v102, v10, v22
	v_mul_f32_e32 v103, v10, v23
	v_mul_f32_e32 v116, v11, v24
	v_mul_f32_e32 v117, v11, v25
	v_mul_f32_e32 v118, v11, v26
	v_mul_f32_e32 v119, v11, v27
	v_add_u32_e32 v6, 0x8000, v6
	global_load_dwordx4 v[224:227], v6, s[12:13] offset:0 nt
	global_load_dwordx4 v[228:231], v6, s[12:13] offset:1024 nt
	global_load_dwordx4 v[232:235], v6, s[12:13] offset:2048 nt
	global_load_dwordx4 v[236:239], v6, s[12:13] offset:3072 nt
	v_add_f32_e32 v16, 0x41800000, v13
	v_add_f32_e32 v17, 0x41880000, v13
	v_add_f32_e32 v18, 0x41900000, v13
	v_add_f32_e32 v19, 0x41980000, v13
	v_mul_f32_e32 v16, v16, v16
	v_mul_f32_e32 v17, v17, v17
	v_mul_f32_e32 v18, v18, v18
	v_mul_f32_e32 v19, v19, v19
	v_mul_f32_e32 v20, v8, v16
	v_mul_f32_e32 v24, v9, v16
	v_mul_f32_e32 v21, v8, v17
	v_mul_f32_e32 v25, v9, v17
	v_mul_f32_e32 v22, v8, v18
	v_mul_f32_e32 v26, v9, v18
	v_mul_f32_e32 v23, v8, v19
	v_mul_f32_e32 v27, v9, v19
	v_exp_f32_e32 v20, v20
	v_exp_f32_e32 v21, v21
	v_exp_f32_e32 v22, v22
	v_exp_f32_e32 v23, v23
	v_exp_f32_e32 v24, v24
	v_exp_f32_e32 v25, v25
	v_exp_f32_e32 v26, v26
	v_exp_f32_e32 v27, v27
	v_mul_f32_e32 v104, v10, v20
	v_mul_f32_e32 v105, v10, v21
	v_mul_f32_e32 v106, v10, v22
	v_mul_f32_e32 v107, v10, v23
	v_mul_f32_e32 v120, v11, v24
	v_mul_f32_e32 v121, v11, v25
	v_mul_f32_e32 v122, v11, v26
	v_mul_f32_e32 v123, v11, v27
	v_add_f32_e32 v16, 0x41c00000, v13
	v_add_f32_e32 v17, 0x41c80000, v13
	v_add_f32_e32 v18, 0x41d00000, v13
	v_add_f32_e32 v19, 0x41d80000, v13
	v_mul_f32_e32 v16, v16, v16
	v_mul_f32_e32 v17, v17, v17
	v_mul_f32_e32 v18, v18, v18
	v_mul_f32_e32 v19, v19, v19
	v_mul_f32_e32 v20, v8, v16
	v_mul_f32_e32 v24, v9, v16
	v_mul_f32_e32 v21, v8, v17
	v_mul_f32_e32 v25, v9, v17
	v_mul_f32_e32 v22, v8, v18
	v_mul_f32_e32 v26, v9, v18
	v_mul_f32_e32 v23, v8, v19
	v_mul_f32_e32 v27, v9, v19
	v_exp_f32_e32 v20, v20
	v_exp_f32_e32 v21, v21
	v_exp_f32_e32 v22, v22
	v_exp_f32_e32 v23, v23
	v_exp_f32_e32 v24, v24
	v_exp_f32_e32 v25, v25
	v_exp_f32_e32 v26, v26
	v_exp_f32_e32 v27, v27
	v_mul_f32_e32 v108, v10, v20
	v_mul_f32_e32 v109, v10, v21
	v_mul_f32_e32 v110, v10, v22
	v_mul_f32_e32 v111, v10, v23
	v_mul_f32_e32 v124, v11, v24
	v_mul_f32_e32 v125, v11, v25
	v_mul_f32_e32 v126, v11, v26
	v_mul_f32_e32 v127, v11, v27
	v_add_u32_e32 v6, 0x8000, v6
	global_load_dwordx4 v[240:243], v6, s[12:13] offset:0 nt
	global_load_dwordx4 v[244:247], v6, s[12:13] offset:1024 nt
	global_load_dwordx4 v[248:251], v6, s[12:13] offset:2048 nt
	global_load_dwordx4 v[252:255], v6, s[12:13] offset:3072 nt
	s_waitcnt vmcnt(28)
	v_add_f32_e32 v128, v128, v129
	v_add_f32_e32 v130, v130, v131
	v_add_f32_e32 v132, v132, v133
	v_add_f32_e32 v134, v134, v135
	v_add_f32_e32 v136, v136, v137
	v_add_f32_e32 v138, v138, v139
	v_add_f32_e32 v140, v140, v141
	v_add_f32_e32 v142, v142, v143
	v_add_f32_e32 v128, v128, v130
	v_add_f32_e32 v132, v132, v134
	v_add_f32_e32 v136, v136, v138
	v_add_f32_e32 v140, v140, v142
	v_cndmask_b32_e64 v130, v128, v132, s[30:31]
	v_cndmask_b32_e64 v134, v136, v140, s[30:31]
	v_cndmask_b32_e64 v129, v132, v128, s[30:31]
	v_cndmask_b32_e64 v133, v140, v136, s[30:31]
	v_add_f32_dpp v129, v130, v129 quad_perm:[1,0,3,2] row_mask:0xf bank_mask:0xf bound_ctrl:1
	v_add_f32_dpp v133, v134, v133 quad_perm:[1,0,3,2] row_mask:0xf bank_mask:0xf bound_ctrl:1
	v_cndmask_b32_e64 v135, v129, v133, s[32:33]
	v_cndmask_b32_e64 v131, v133, v129, s[32:33]
	s_nop 1
	v_add_f32_dpp v131, v135, v131 quad_perm:[2,3,0,1] row_mask:0xf bank_mask:0xf bound_ctrl:1
	v_cvt_f16_f32_e32 v131, v131
	ds_write_b16 v14, v131 offset:0
	s_waitcnt vmcnt(24)
	v_add_f32_e32 v144, v144, v145
	v_add_f32_e32 v146, v146, v147
	v_add_f32_e32 v148, v148, v149
	v_add_f32_e32 v150, v150, v151
	v_add_f32_e32 v152, v152, v153
	v_add_f32_e32 v154, v154, v155
	v_add_f32_e32 v156, v156, v157
	v_add_f32_e32 v158, v158, v159
	v_add_f32_e32 v144, v144, v146
	v_add_f32_e32 v148, v148, v150
	v_add_f32_e32 v152, v152, v154
	v_add_f32_e32 v156, v156, v158
	v_cndmask_b32_e64 v146, v144, v148, s[30:31]
	v_cndmask_b32_e64 v150, v152, v156, s[30:31]
	v_cndmask_b32_e64 v145, v148, v144, s[30:31]
	v_cndmask_b32_e64 v149, v156, v152, s[30:31]
	v_add_f32_dpp v145, v146, v145 quad_perm:[1,0,3,2] row_mask:0xf bank_mask:0xf bound_ctrl:1
	v_add_f32_dpp v149, v150, v149 quad_perm:[1,0,3,2] row_mask:0xf bank_mask:0xf bound_ctrl:1
	v_cndmask_b32_e64 v151, v145, v149, s[32:33]
	v_cndmask_b32_e64 v147, v149, v145, s[32:33]
	s_nop 1
	v_add_f32_dpp v147, v151, v147 quad_perm:[2,3,0,1] row_mask:0xf bank_mask:0xf bound_ctrl:1
	v_cvt_f16_f32_e32 v147, v147
	ds_write_b16 v14, v147 offset:1088
	s_waitcnt vmcnt(20)
	v_add_f32_e32 v160, v160, v161
	v_add_f32_e32 v162, v162, v163
	v_add_f32_e32 v164, v164, v165
	v_add_f32_e32 v166, v166, v167
	v_add_f32_e32 v168, v168, v169
	v_add_f32_e32 v170, v170, v171
	v_add_f32_e32 v172, v172, v173
	v_add_f32_e32 v174, v174, v175
	v_add_f32_e32 v160, v160, v162
	v_add_f32_e32 v164, v164, v166
	v_add_f32_e32 v168, v168, v170
	v_add_f32_e32 v172, v172, v174
	v_cndmask_b32_e64 v162, v160, v164, s[30:31]
	v_cndmask_b32_e64 v166, v168, v172, s[30:31]
	v_cndmask_b32_e64 v161, v164, v160, s[30:31]
	v_cndmask_b32_e64 v165, v172, v168, s[30:31]
	v_add_f32_dpp v161, v162, v161 quad_perm:[1,0,3,2] row_mask:0xf bank_mask:0xf bound_ctrl:1
	v_add_f32_dpp v165, v166, v165 quad_perm:[1,0,3,2] row_mask:0xf bank_mask:0xf bound_ctrl:1
	v_cndmask_b32_e64 v167, v161, v165, s[32:33]
	v_cndmask_b32_e64 v163, v165, v161, s[32:33]
	s_nop 1
	v_add_f32_dpp v163, v167, v163 quad_perm:[2,3,0,1] row_mask:0xf bank_mask:0xf bound_ctrl:1
	v_cvt_f16_f32_e32 v163, v163
	ds_write_b16 v14, v163 offset:2176
	s_waitcnt vmcnt(16)
	v_add_f32_e32 v176, v176, v177
	v_add_f32_e32 v178, v178, v179
	v_add_f32_e32 v180, v180, v181
	v_add_f32_e32 v182, v182, v183
	v_add_f32_e32 v184, v184, v185
	v_add_f32_e32 v186, v186, v187
	v_add_f32_e32 v188, v188, v189
	v_add_f32_e32 v190, v190, v191
	v_add_f32_e32 v176, v176, v178
	v_add_f32_e32 v180, v180, v182
	v_add_f32_e32 v184, v184, v186
	v_add_f32_e32 v188, v188, v190
	v_cndmask_b32_e64 v178, v176, v180, s[30:31]
	v_cndmask_b32_e64 v182, v184, v188, s[30:31]
	v_cndmask_b32_e64 v177, v180, v176, s[30:31]
	v_cndmask_b32_e64 v181, v188, v184, s[30:31]
	v_add_f32_dpp v177, v178, v177 quad_perm:[1,0,3,2] row_mask:0xf bank_mask:0xf bound_ctrl:1
	v_add_f32_dpp v181, v182, v181 quad_perm:[1,0,3,2] row_mask:0xf bank_mask:0xf bound_ctrl:1
	v_cndmask_b32_e64 v183, v177, v181, s[32:33]
	v_cndmask_b32_e64 v179, v181, v177, s[32:33]
	s_nop 1
	v_add_f32_dpp v179, v183, v179 quad_perm:[2,3,0,1] row_mask:0xf bank_mask:0xf bound_ctrl:1
	v_cvt_f16_f32_e32 v179, v179
	ds_write_b16 v14, v179 offset:3264
	s_waitcnt vmcnt(12)
	v_add_f32_e32 v192, v192, v193
	v_add_f32_e32 v194, v194, v195
	v_add_f32_e32 v196, v196, v197
	v_add_f32_e32 v198, v198, v199
	v_add_f32_e32 v200, v200, v201
	v_add_f32_e32 v202, v202, v203
	v_add_f32_e32 v204, v204, v205
	v_add_f32_e32 v206, v206, v207
	v_add_f32_e32 v192, v192, v194
	v_add_f32_e32 v196, v196, v198
	v_add_f32_e32 v200, v200, v202
	v_add_f32_e32 v204, v204, v206
	v_cndmask_b32_e64 v194, v192, v196, s[30:31]
	v_cndmask_b32_e64 v198, v200, v204, s[30:31]
	v_cndmask_b32_e64 v193, v196, v192, s[30:31]
	v_cndmask_b32_e64 v197, v204, v200, s[30:31]
	v_add_f32_dpp v193, v194, v193 quad_perm:[1,0,3,2] row_mask:0xf bank_mask:0xf bound_ctrl:1
	v_add_f32_dpp v197, v198, v197 quad_perm:[1,0,3,2] row_mask:0xf bank_mask:0xf bound_ctrl:1
	v_cndmask_b32_e64 v199, v193, v197, s[32:33]
	v_cndmask_b32_e64 v195, v197, v193, s[32:33]
	s_nop 1
	v_add_f32_dpp v195, v199, v195 quad_perm:[2,3,0,1] row_mask:0xf bank_mask:0xf bound_ctrl:1
	v_cvt_f16_f32_e32 v195, v195
	ds_write_b16 v14, v195 offset:4352
	s_waitcnt vmcnt(8)
	v_add_f32_e32 v208, v208, v209
	v_add_f32_e32 v210, v210, v211
	v_add_f32_e32 v212, v212, v213
	v_add_f32_e32 v214, v214, v215
	v_add_f32_e32 v216, v216, v217
	v_add_f32_e32 v218, v218, v219
	v_add_f32_e32 v220, v220, v221
	v_add_f32_e32 v222, v222, v223
	v_add_f32_e32 v208, v208, v210
	v_add_f32_e32 v212, v212, v214
	v_add_f32_e32 v216, v216, v218
	v_add_f32_e32 v220, v220, v222
	v_cndmask_b32_e64 v210, v208, v212, s[30:31]
	v_cndmask_b32_e64 v214, v216, v220, s[30:31]
	v_cndmask_b32_e64 v209, v212, v208, s[30:31]
	v_cndmask_b32_e64 v213, v220, v216, s[30:31]
	v_add_f32_dpp v209, v210, v209 quad_perm:[1,0,3,2] row_mask:0xf bank_mask:0xf bound_ctrl:1
	v_add_f32_dpp v213, v214, v213 quad_perm:[1,0,3,2] row_mask:0xf bank_mask:0xf bound_ctrl:1
	v_cndmask_b32_e64 v215, v209, v213, s[32:33]
	v_cndmask_b32_e64 v211, v213, v209, s[32:33]
	s_nop 1
	v_add_f32_dpp v211, v215, v211 quad_perm:[2,3,0,1] row_mask:0xf bank_mask:0xf bound_ctrl:1
	v_cvt_f16_f32_e32 v211, v211
	ds_write_b16 v14, v211 offset:5440
	s_waitcnt vmcnt(4)
	v_add_f32_e32 v224, v224, v225
	v_add_f32_e32 v226, v226, v227
	v_add_f32_e32 v228, v228, v229
	v_add_f32_e32 v230, v230, v231
	v_add_f32_e32 v232, v232, v233
	v_add_f32_e32 v234, v234, v235
	v_add_f32_e32 v236, v236, v237
	v_add_f32_e32 v238, v238, v239
	v_add_f32_e32 v224, v224, v226
	v_add_f32_e32 v228, v228, v230
	v_add_f32_e32 v232, v232, v234
	v_add_f32_e32 v236, v236, v238
	v_cndmask_b32_e64 v226, v224, v228, s[30:31]
	v_cndmask_b32_e64 v230, v232, v236, s[30:31]
	v_cndmask_b32_e64 v225, v228, v224, s[30:31]
	v_cndmask_b32_e64 v229, v236, v232, s[30:31]
	v_add_f32_dpp v225, v226, v225 quad_perm:[1,0,3,2] row_mask:0xf bank_mask:0xf bound_ctrl:1
	v_add_f32_dpp v229, v230, v229 quad_perm:[1,0,3,2] row_mask:0xf bank_mask:0xf bound_ctrl:1
	v_cndmask_b32_e64 v231, v225, v229, s[32:33]
	v_cndmask_b32_e64 v227, v229, v225, s[32:33]
	s_nop 1
	v_add_f32_dpp v227, v231, v227 quad_perm:[2,3,0,1] row_mask:0xf bank_mask:0xf bound_ctrl:1
	v_cvt_f16_f32_e32 v227, v227
	ds_write_b16 v14, v227 offset:6528
	s_waitcnt vmcnt(0)
	v_add_f32_e32 v240, v240, v241
	v_add_f32_e32 v242, v242, v243
	v_add_f32_e32 v244, v244, v245
	v_add_f32_e32 v246, v246, v247
	v_add_f32_e32 v248, v248, v249
	v_add_f32_e32 v250, v250, v251
	v_add_f32_e32 v252, v252, v253
	v_add_f32_e32 v254, v254, v255
	v_add_f32_e32 v240, v240, v242
	v_add_f32_e32 v244, v244, v246
	v_add_f32_e32 v248, v248, v250
	v_add_f32_e32 v252, v252, v254
	v_cndmask_b32_e64 v242, v240, v244, s[30:31]
	v_cndmask_b32_e64 v246, v248, v252, s[30:31]
	v_cndmask_b32_e64 v241, v244, v240, s[30:31]
	v_cndmask_b32_e64 v245, v252, v248, s[30:31]
	v_add_f32_dpp v241, v242, v241 quad_perm:[1,0,3,2] row_mask:0xf bank_mask:0xf bound_ctrl:1
	v_add_f32_dpp v245, v246, v245 quad_perm:[1,0,3,2] row_mask:0xf bank_mask:0xf bound_ctrl:1
	v_cndmask_b32_e64 v247, v241, v245, s[32:33]
	v_cndmask_b32_e64 v243, v245, v241, s[32:33]
	s_nop 1
	v_add_f32_dpp v243, v247, v243 quad_perm:[2,3,0,1] row_mask:0xf bank_mask:0xf bound_ctrl:1
	v_cvt_f16_f32_e32 v243, v243
	ds_write_b16 v14, v243 offset:7616
	s_waitcnt lgkmcnt(0)
	s_barrier
	ds_read_b128 v[160:163], v15 offset:0
	ds_read_b128 v[164:167], v15 offset:32
	ds_read_b128 v[168:171], v15 offset:64
	ds_read_b128 v[172:175], v15 offset:96
	ds_read_b128 v[176:179], v15 offset:128
	ds_read_b128 v[180:183], v15 offset:160
	ds_read_b128 v[184:187], v15 offset:192
	ds_read_b128 v[188:191], v15 offset:224
	s_waitcnt lgkmcnt(7)
	v_mfma_f32_32x32x16_f16 v[128:143], v[160:163], v[32:35], 0
	v_mfma_f32_32x32x16_f16 v[144:159], v[160:163], v[64:67], 0
	s_waitcnt lgkmcnt(6)
	v_mfma_f32_32x32x16_f16 v[128:143], v[164:167], v[36:39], v[128:143]
	v_mfma_f32_32x32x16_f16 v[144:159], v[164:167], v[68:71], v[144:159]
	s_waitcnt lgkmcnt(5)
	v_mfma_f32_32x32x16_f16 v[128:143], v[168:171], v[40:43], v[128:143]
	v_mfma_f32_32x32x16_f16 v[144:159], v[168:171], v[72:75], v[144:159]
	s_waitcnt lgkmcnt(4)
	v_mfma_f32_32x32x16_f16 v[128:143], v[172:175], v[44:47], v[128:143]
	v_mfma_f32_32x32x16_f16 v[144:159], v[172:175], v[76:79], v[144:159]
	s_waitcnt lgkmcnt(3)
	v_mfma_f32_32x32x16_f16 v[128:143], v[176:179], v[48:51], v[128:143]
	v_mfma_f32_32x32x16_f16 v[144:159], v[176:179], v[80:83], v[144:159]
	s_waitcnt lgkmcnt(2)
	v_mfma_f32_32x32x16_f16 v[128:143], v[180:183], v[52:55], v[128:143]
	v_mfma_f32_32x32x16_f16 v[144:159], v[180:183], v[84:87], v[144:159]
	s_waitcnt lgkmcnt(1)
	v_mfma_f32_32x32x16_f16 v[128:143], v[184:187], v[56:59], v[128:143]
	v_mfma_f32_32x32x16_f16 v[144:159], v[184:187], v[88:91], v[144:159]
	s_waitcnt lgkmcnt(0)
	v_mfma_f32_32x32x16_f16 v[128:143], v[188:191], v[60:63], v[128:143]
	v_mfma_f32_32x32x16_f16 v[144:159], v[188:191], v[92:95], v[144:159]
	s_nop 15
	s_nop 3
	v_mul_f32_e32 v16, v96, v128
	v_mul_f32_e32 v17, v97, v129
	v_mul_f32_e32 v18, v98, v130
	v_mul_f32_e32 v19, v99, v131
	v_fma_f32 v16, -v112, v144, v16
	v_fma_f32 v17, -v113, v145, v17
	v_fma_f32 v18, -v114, v146, v18
	v_fma_f32 v19, -v115, v147, v19
	v_fma_f32 v16, v100, v132, v16
	v_fma_f32 v16, -v116, v148, v16
	v_fma_f32 v17, v101, v133, v17
	v_fma_f32 v17, -v117, v149, v17
	v_fma_f32 v18, v102, v134, v18
	v_fma_f32 v18, -v118, v150, v18
	v_fma_f32 v19, v103, v135, v19
	v_fma_f32 v19, -v119, v151, v19
	v_fma_f32 v16, v104, v136, v16
	v_fma_f32 v16, -v120, v152, v16
	v_fma_f32 v17, v105, v137, v17
	v_fma_f32 v17, -v121, v153, v17
	v_fma_f32 v18, v106, v138, v18
	v_fma_f32 v18, -v122, v154, v18
	v_fma_f32 v19, v107, v139, v19
	v_fma_f32 v19, -v123, v155, v19
	v_fma_f32 v16, v108, v140, v16
	v_fma_f32 v16, -v124, v156, v16
	v_fma_f32 v17, v109, v141, v17
	v_fma_f32 v17, -v125, v157, v17
	v_fma_f32 v18, v110, v142, v18
	v_fma_f32 v18, -v126, v158, v18
	v_fma_f32 v19, v111, v143, v19
	v_fma_f32 v19, -v127, v159, v19
	v_add_f32_e32 v16, v16, v17
	v_add_f32_e32 v18, v18, v19
	v_add_f32_e32 v16, v16, v18
	v_mov_b32_e32 v17, v16
	s_lshl_b32 s6, s6, 6
	s_add_i32 s6, s6, s7
	s_lshl_b32 s6, s6, 10
	v_permlane32_swap_b32_e32 v16, v17
	v_add_u32_e32 v5, s6, v5
	v_cmp_gt_u32_e32 vcc, 32, v1
	v_add_f32_e32 v16, v16, v17
	s_and_saveexec_b64 s[2:3], vcc
	s_cbranch_execz .Ldog_main_done
	global_store_dword v5, v16, s[26:27]
